# sort blocks of k_bucket also convert one x->fp16 unit each while their edge loads are in flight
# speedup vs baseline: 1.0193x; 1.0090x over previous
_Z8k_bucketPKiS0_PKjPiS3_PK15HIP_vector_typeIfLj4EEPS4_IjLj4EE:
	s_load_dword s66, s[0:1], 0x0
	s_load_dword s67, s[0:1], 0x40
	v_lshrrev_b32_e32 v1, 6, v0
	s_nop 0
	v_readfirstlane_b32 s65, v1
	s_cmpk_ge_u32 s2, 585
	s_cbranch_scc1 .Lmy_cvt1_end
	s_movk_i32 s64, 0x5aa5
	s_mov_b64 exec, 0
	s_cmpk_lt_u32 s65, 8
	s_cbranch_scc1 .Lw1s0d0_16
	s_cmpk_lt_u32 s65, 12
	s_cbranch_scc1 .Lw1s0d8_16
	s_cmpk_lt_u32 s65, 14
	s_cbranch_scc1 .Lw1s0d12_16
	s_cmpk_lt_u32 s65, 15
	s_cbranch_scc1 .Lw1s0d14_16
	s_branch .Lw1t15

.Lw1b33:
	s_movk_i32 s57, 0x2000
	s_and_b64 vcc, exec, s[34:35]
	s_cbranch_vccz .LBB1_231
	s_waitcnt lgkmcnt(0)
	s_load_dwordx4 s[68:71], s[0:1], 0x28
	s_and_b64 s[36:37], s[30:31], exec
	s_cselect_b32 s72, 0xc4, 0
	s_add_i32 s72, s72, s33
	s_addk_i32 s72, 0x190
	v_and_b32_e32 v48, 0x3c0, v0
	v_and_b32_e32 v49, 63, v0

.Lw1b34:
	v_lshlrev_b32_e32 v58, 5, v48
	v_lshl_or_b32 v58, v49, 4, v58
	v_and_b32_e32 v59, 1, v0
	v_lshrrev_b32_e32 v49, 1, v49
	v_lshl_or_b32 v49, v59, 5, v49
	v_add_u32_e32 v49, v49, v48
	v_lshlrev_b32_e32 v49, 4, v49
	s_lshl_b32 s73, s72, 15
	s_waitcnt lgkmcnt(0)
	s_add_u32 s68, s68, s73
	s_addc_u32 s69, s69, 0
	s_mov_b32 s34, 0x11800

.Lw1b35:
	s_movk_i32 s35, 0x62
	v_mov_b32_e32 v32, v0
	v_add_u32_e32 v33, 1024, v0
	v_add_u32_e32 v34, 2048, v0
	v_add_u32_e32 v35, 3072, v0
	v_add_u32_e32 v36, 4096, v0
	v_add_u32_e32 v37, 5120, v0
	v_add_u32_e32 v38, 6144, v0
	v_add_u32_e32 v39, 7168, v0

.Lw1b36:
	v_cmp_le_i32_e64 s[36:37], v5, v32
	v_cmp_le_i32_e64 s[38:39], v5, v33
	v_cmp_le_i32_e64 s[58:59], v5, v34
	v_cmp_le_i32_e64 s[60:61], v5, v35
	v_cndmask_b32_e64 v40, 0, 64, s[36:37]
	v_cndmask_b32_e64 v41, 0, 64, s[38:39]
	v_cndmask_b32_e64 v42, 0, 64, s[58:59]

.Lw1b37:
	v_cndmask_b32_e64 v43, 0, 64, s[60:61]
	v_cmp_le_i32_e64 s[36:37], v5, v36
	v_cmp_le_i32_e64 s[38:39], v5, v37
	v_cmp_le_i32_e64 s[58:59], v5, v38
	v_cmp_le_i32_e64 s[60:61], v5, v39
	v_cndmask_b32_e64 v44, 0, 64, s[36:37]
	v_cndmask_b32_e64 v45, 0, 64, s[38:39]
	v_cndmask_b32_e64 v46, 0, 64, s[58:59]

.Lw1b38:
	v_cndmask_b32_e64 v47, 0, 64, s[60:61]
	v_add_u32_e32 v3, 32, v40
	v_lshl_add_u32 v11, v3, 2, s34
	ds_read_b32 v11, v11
	v_add_u32_e32 v4, 32, v41
	v_lshl_add_u32 v12, v4, 2, s34
	ds_read_b32 v12, v12
	v_add_u32_e32 v6, 32, v42
	v_lshl_add_u32 v13, v6, 2, s34

.Lw1b39:
	ds_read_b32 v13, v13
	v_add_u32_e32 v7, 32, v43
	v_lshl_add_u32 v14, v7, 2, s34
	ds_read_b32 v14, v14
	v_add_u32_e32 v8, 32, v44
	v_lshl_add_u32 v15, v8, 2, s34
	ds_read_b32 v15, v15
	v_add_u32_e32 v9, 32, v45
	v_lshl_add_u32 v16, v9, 2, s34

.Lw1b40:
	ds_read_b32 v16, v16
	v_add_u32_e32 v10, 32, v46
	v_lshl_add_u32 v17, v10, 2, s34
	ds_read_b32 v17, v17
	v_add_u32_e32 v19, 32, v47
	v_lshl_add_u32 v18, v19, 2, s34
	ds_read_b32 v18, v18
	s_waitcnt lgkmcnt(7)
	v_cmp_le_i32_e64 s[36:37], v11, v32

.Lw1b42:
	v_cndmask_b32_e64 v43, v43, v7, s[60:61]
	s_waitcnt lgkmcnt(3)
	v_cmp_le_i32_e64 s[36:37], v15, v36
	s_waitcnt lgkmcnt(2)
	v_cmp_le_i32_e64 s[38:39], v16, v37
	s_waitcnt lgkmcnt(1)
	v_cmp_le_i32_e64 s[58:59], v17, v38
	s_waitcnt lgkmcnt(0)
	v_cmp_le_i32_e64 s[60:61], v18, v39
.Lw1t43:
	s_cbranch_execz .Lw1c43
.Lw1b43:
	v_cndmask_b32_e64 v44, v44, v8, s[36:37]
	v_cndmask_b32_e64 v45, v45, v9, s[38:39]
	v_cndmask_b32_e64 v46, v46, v10, s[58:59]
	v_cndmask_b32_e64 v47, v47, v19, s[60:61]
	v_add_u32_e32 v3, 16, v40
	v_min_u32_e32 v11, s35, v3
	v_lshl_add_u32 v11, v11, 2, s34
	ds_read_b32 v11, v11
	v_add_u32_e32 v4, 16, v41

.Lw1b44:
	v_min_u32_e32 v12, s35, v4
	v_lshl_add_u32 v12, v12, 2, s34
	ds_read_b32 v12, v12
	v_add_u32_e32 v6, 16, v42
	v_min_u32_e32 v13, s35, v6
	v_lshl_add_u32 v13, v13, 2, s34
	ds_read_b32 v13, v13
	v_add_u32_e32 v7, 16, v43
	v_min_u32_e32 v14, s35, v7
	v_lshl_add_u32 v14, v14, 2, s34

.Lw1b45:
	ds_read_b32 v14, v14
	v_add_u32_e32 v8, 16, v44
	v_min_u32_e32 v15, s35, v8
	v_lshl_add_u32 v15, v15, 2, s34
	ds_read_b32 v15, v15
	v_add_u32_e32 v9, 16, v45
	v_min_u32_e32 v16, s35, v9
	v_lshl_add_u32 v16, v16, 2, s34
	ds_read_b32 v16, v16
	v_add_u32_e32 v10, 16, v46

.Lw1b46:
	v_min_u32_e32 v17, s35, v10
	v_lshl_add_u32 v17, v17, 2, s34
	ds_read_b32 v17, v17
	v_add_u32_e32 v19, 16, v47
	v_min_u32_e32 v18, s35, v19
	v_lshl_add_u32 v18, v18, 2, s34
	ds_read_b32 v18, v18
	s_waitcnt lgkmcnt(7)
	v_cmp_le_i32_e64 s[36:37], v11, v32
	s_waitcnt lgkmcnt(6)

.Lw1b47:
	v_cmp_le_i32_e64 s[38:39], v12, v33
	s_waitcnt lgkmcnt(5)
	v_cmp_le_i32_e64 s[58:59], v13, v34
	s_waitcnt lgkmcnt(4)
	v_cmp_le_i32_e64 s[60:61], v14, v35
	v_cndmask_b32_e64 v40, v40, v3, s[36:37]
	v_cndmask_b32_e64 v41, v41, v4, s[38:39]
	v_cndmask_b32_e64 v42, v42, v6, s[58:59]
	v_cndmask_b32_e64 v43, v43, v7, s[60:61]

.Lw1b48:
	s_waitcnt lgkmcnt(3)
	v_cmp_le_i32_e64 s[36:37], v15, v36
	s_waitcnt lgkmcnt(2)
	v_cmp_le_i32_e64 s[38:39], v16, v37
	s_waitcnt lgkmcnt(1)
	v_cmp_le_i32_e64 s[58:59], v17, v38
	s_waitcnt lgkmcnt(0)
	v_cmp_le_i32_e64 s[60:61], v18, v39
	v_cndmask_b32_e64 v44, v44, v8, s[36:37]
.Lw1t49:
	s_cbranch_execz .Lw1c49
.Lw1b49:
	v_cndmask_b32_e64 v45, v45, v9, s[38:39]
	v_cndmask_b32_e64 v46, v46, v10, s[58:59]
	v_cndmask_b32_e64 v47, v47, v19, s[60:61]
	v_add_u32_e32 v3, 8, v40
	v_min_u32_e32 v11, s35, v3
	v_lshl_add_u32 v11, v11, 2, s34
	ds_read_b32 v11, v11
	v_add_u32_e32 v4, 8, v41
	v_min_u32_e32 v12, s35, v4
	v_lshl_add_u32 v12, v12, 2, s34

.Lw1b50:
	ds_read_b32 v12, v12
	v_add_u32_e32 v6, 8, v42
	v_min_u32_e32 v13, s35, v6
	v_lshl_add_u32 v13, v13, 2, s34
	ds_read_b32 v13, v13
	v_add_u32_e32 v7, 8, v43
	v_min_u32_e32 v14, s35, v7
	v_lshl_add_u32 v14, v14, 2, s34
	ds_read_b32 v14, v14

.Lw1b51:
	v_add_u32_e32 v8, 8, v44
	v_min_u32_e32 v15, s35, v8
	v_lshl_add_u32 v15, v15, 2, s34
	ds_read_b32 v15, v15
	v_add_u32_e32 v9, 8, v45
	v_min_u32_e32 v16, s35, v9
	v_lshl_add_u32 v16, v16, 2, s34
	ds_read_b32 v16, v16
	v_add_u32_e32 v10, 8, v46
	v_min_u32_e32 v17, s35, v10
	v_lshl_add_u32 v17, v17, 2, s34

.Lw1b52:
	ds_read_b32 v17, v17
	v_add_u32_e32 v19, 8, v47
	v_min_u32_e32 v18, s35, v19
	v_lshl_add_u32 v18, v18, 2, s34
	ds_read_b32 v18, v18
	s_waitcnt lgkmcnt(7)
	v_cmp_le_i32_e64 s[36:37], v11, v32
	s_waitcnt lgkmcnt(6)
	v_cmp_le_i32_e64 s[38:39], v12, v33

.Lw1b53:
	s_waitcnt lgkmcnt(5)
	v_cmp_le_i32_e64 s[58:59], v13, v34
	s_waitcnt lgkmcnt(4)
	v_cmp_le_i32_e64 s[60:61], v14, v35
	v_cndmask_b32_e64 v40, v40, v3, s[36:37]
	v_cndmask_b32_e64 v41, v41, v4, s[38:39]
	v_cndmask_b32_e64 v42, v42, v6, s[58:59]
	v_cndmask_b32_e64 v43, v43, v7, s[60:61]
	s_waitcnt lgkmcnt(3)

.Lw1b54:
	v_cmp_le_i32_e64 s[36:37], v15, v36
	s_waitcnt lgkmcnt(2)
	v_cmp_le_i32_e64 s[38:39], v16, v37
	s_waitcnt lgkmcnt(1)
	v_cmp_le_i32_e64 s[58:59], v17, v38
	s_waitcnt lgkmcnt(0)
	v_cmp_le_i32_e64 s[60:61], v18, v39
	v_cndmask_b32_e64 v44, v44, v8, s[36:37]
	v_cndmask_b32_e64 v45, v45, v9, s[38:39]

.Lw1b55:
	v_cndmask_b32_e64 v46, v46, v10, s[58:59]
	v_cndmask_b32_e64 v47, v47, v19, s[60:61]
	v_add_u32_e32 v3, 4, v40
	v_min_u32_e32 v11, s35, v3
	v_lshl_add_u32 v11, v11, 2, s34
	ds_read_b32 v11, v11
	v_add_u32_e32 v4, 4, v41
	v_min_u32_e32 v12, s35, v4
	v_lshl_add_u32 v12, v12, 2, s34
	ds_read_b32 v12, v12

.Lw1b56:
	v_add_u32_e32 v6, 4, v42
	v_min_u32_e32 v13, s35, v6
	v_lshl_add_u32 v13, v13, 2, s34
	ds_read_b32 v13, v13
	v_add_u32_e32 v7, 4, v43
	v_min_u32_e32 v14, s35, v7
	v_lshl_add_u32 v14, v14, 2, s34
	ds_read_b32 v14, v14
	v_add_u32_e32 v8, 4, v44
	v_min_u32_e32 v15, s35, v8

.Lw1b57:
	v_lshl_add_u32 v15, v15, 2, s34
	ds_read_b32 v15, v15
	v_add_u32_e32 v9, 4, v45
	v_min_u32_e32 v16, s35, v9
	v_lshl_add_u32 v16, v16, 2, s34
	ds_read_b32 v16, v16
	v_add_u32_e32 v10, 4, v46
	v_min_u32_e32 v17, s35, v10
	v_lshl_add_u32 v17, v17, 2, s34
	ds_read_b32 v17, v17

.Lw1b58:
	v_add_u32_e32 v19, 4, v47
	v_min_u32_e32 v18, s35, v19
	v_lshl_add_u32 v18, v18, 2, s34
	ds_read_b32 v18, v18
	s_waitcnt lgkmcnt(7)
	v_cmp_le_i32_e64 s[36:37], v11, v32
	s_waitcnt lgkmcnt(6)
	v_cmp_le_i32_e64 s[38:39], v12, v33
	s_waitcnt lgkmcnt(5)
	v_cmp_le_i32_e64 s[58:59], v13, v34

.Lw1b59:
	s_waitcnt lgkmcnt(4)
	v_cmp_le_i32_e64 s[60:61], v14, v35
	v_cndmask_b32_e64 v40, v40, v3, s[36:37]
	v_cndmask_b32_e64 v41, v41, v4, s[38:39]
	v_cndmask_b32_e64 v42, v42, v6, s[58:59]
	v_cndmask_b32_e64 v43, v43, v7, s[60:61]
	s_waitcnt lgkmcnt(3)
	v_cmp_le_i32_e64 s[36:37], v15, v36

.Lw1b60:
	s_waitcnt lgkmcnt(2)
	v_cmp_le_i32_e64 s[38:39], v16, v37
	s_waitcnt lgkmcnt(1)
	v_cmp_le_i32_e64 s[58:59], v17, v38
	s_waitcnt lgkmcnt(0)
	v_cmp_le_i32_e64 s[60:61], v18, v39
	v_cndmask_b32_e64 v44, v44, v8, s[36:37]
	v_cndmask_b32_e64 v45, v45, v9, s[38:39]
	v_cndmask_b32_e64 v46, v46, v10, s[58:59]

.Lw1b61:
	v_cndmask_b32_e64 v47, v47, v19, s[60:61]
	v_add_u32_e32 v3, 2, v40
	v_min_u32_e32 v11, s35, v3
	v_lshl_add_u32 v11, v11, 2, s34
	ds_read_b32 v11, v11
	v_add_u32_e32 v4, 2, v41
	v_min_u32_e32 v12, s35, v4
	v_lshl_add_u32 v12, v12, 2, s34
	ds_read_b32 v12, v12
	v_add_u32_e32 v6, 2, v42

.Lw1b62:
	v_min_u32_e32 v13, s35, v6
	v_lshl_add_u32 v13, v13, 2, s34
	ds_read_b32 v13, v13
	v_add_u32_e32 v7, 2, v43
	v_min_u32_e32 v14, s35, v7
	v_lshl_add_u32 v14, v14, 2, s34
	ds_read_b32 v14, v14
	v_add_u32_e32 v8, 2, v44
	v_min_u32_e32 v15, s35, v8
	v_lshl_add_u32 v15, v15, 2, s34

.Lw1b63:
	ds_read_b32 v15, v15
	v_add_u32_e32 v9, 2, v45
	v_min_u32_e32 v16, s35, v9
	v_lshl_add_u32 v16, v16, 2, s34
	ds_read_b32 v16, v16
	v_add_u32_e32 v10, 2, v46
	v_min_u32_e32 v17, s35, v10
	v_lshl_add_u32 v17, v17, 2, s34
	ds_read_b32 v17, v17
	v_add_u32_e32 v19, 2, v47

.Lw1b64:
	v_min_u32_e32 v18, s35, v19
	v_lshl_add_u32 v18, v18, 2, s34
	ds_read_b32 v18, v18
	s_waitcnt lgkmcnt(7)
	v_cmp_le_i32_e64 s[36:37], v11, v32
	s_waitcnt lgkmcnt(6)
	v_cmp_le_i32_e64 s[38:39], v12, v33
	s_waitcnt lgkmcnt(5)
	v_cmp_le_i32_e64 s[58:59], v13, v34
	s_waitcnt lgkmcnt(4)

.Lw1b67:
	v_add_u32_e32 v3, 1, v40
	v_min_u32_e32 v11, s35, v3
	v_lshl_add_u32 v11, v11, 2, s34
	ds_read_b32 v11, v11
	v_add_u32_e32 v4, 1, v41
	v_min_u32_e32 v12, s35, v4
	v_lshl_add_u32 v12, v12, 2, s34
	ds_read_b32 v12, v12
	v_add_u32_e32 v6, 1, v42
	v_min_u32_e32 v13, s35, v6
	v_lshl_add_u32 v13, v13, 2, s34

.Lw1b68:
	ds_read_b32 v13, v13
	v_add_u32_e32 v7, 1, v43
	v_min_u32_e32 v14, s35, v7
	v_lshl_add_u32 v14, v14, 2, s34
	ds_read_b32 v14, v14
	v_add_u32_e32 v8, 1, v44
	v_min_u32_e32 v15, s35, v8
	v_lshl_add_u32 v15, v15, 2, s34
	ds_read_b32 v15, v15

.Lw1b69:
	v_add_u32_e32 v9, 1, v45
	v_min_u32_e32 v16, s35, v9
	v_lshl_add_u32 v16, v16, 2, s34
	ds_read_b32 v16, v16
	v_add_u32_e32 v10, 1, v46
	v_min_u32_e32 v17, s35, v10
	v_lshl_add_u32 v17, v17, 2, s34
	ds_read_b32 v17, v17
	v_add_u32_e32 v19, 1, v47
	v_min_u32_e32 v18, s35, v19
	v_lshl_add_u32 v18, v18, 2, s34

.Lw1b72:
	v_cmp_le_i32_e64 s[58:59], v17, v38
	s_waitcnt lgkmcnt(0)
	v_cmp_le_i32_e64 s[60:61], v18, v39
	v_cndmask_b32_e64 v44, v44, v8, s[36:37]
	v_cndmask_b32_e64 v45, v45, v9, s[38:39]
	v_cndmask_b32_e64 v46, v46, v10, s[58:59]
	v_cndmask_b32_e64 v47, v47, v19, s[60:61]
	v_lshl_add_u32 v11, v40, 2, s34

.Lw1b73:
	ds_read_b32 v3, v11
	ds_read_b32 v11, v11 offset:400
	v_lshl_add_u32 v12, v41, 2, s34
	ds_read_b32 v4, v12
	ds_read_b32 v12, v12 offset:400
	v_lshl_add_u32 v13, v42, 2, s34
	ds_read_b32 v6, v13
	ds_read_b32 v13, v13 offset:400

.Lw1b74:
	v_lshl_add_u32 v14, v43, 2, s34
	ds_read_b32 v7, v14
	ds_read_b32 v14, v14 offset:400
	v_lshl_add_u32 v15, v44, 2, s34
	ds_read_b32 v8, v15
	ds_read_b32 v15, v15 offset:400
	v_lshl_add_u32 v16, v45, 2, s34

.Lw1b75:
	ds_read_b32 v9, v16
	ds_read_b32 v16, v16 offset:400
	v_lshl_add_u32 v17, v46, 2, s34
	ds_read_b32 v10, v17
	ds_read_b32 v17, v17 offset:400
	v_lshl_add_u32 v18, v47, 2, s34
	ds_read_b32 v19, v18
	ds_read_b32 v18, v18 offset:400

.Lw1b76:
	s_waitcnt lgkmcnt(14)
	v_sub_u32_e32 v3, v32, v3
	v_lshl_add_u32 v40, v40, 13, v3
	v_add_lshl_u32 v40, v40, v11, 2
	s_waitcnt lgkmcnt(12)
	v_sub_u32_e32 v4, v33, v4
	v_lshl_add_u32 v41, v41, 13, v4
	v_add_lshl_u32 v41, v41, v12, 2
	s_waitcnt lgkmcnt(10)
	v_sub_u32_e32 v6, v34, v6

.Lw1b77:
	v_lshl_add_u32 v42, v42, 13, v6
	v_add_lshl_u32 v42, v42, v13, 2
	s_waitcnt lgkmcnt(8)
	v_sub_u32_e32 v7, v35, v7
	v_lshl_add_u32 v43, v43, 13, v7
	v_add_lshl_u32 v43, v43, v14, 2
	s_waitcnt lgkmcnt(6)
	v_sub_u32_e32 v8, v36, v8
	v_lshl_add_u32 v44, v44, 13, v8
	v_add_lshl_u32 v44, v44, v15, 2

.Lw1b78:
	s_waitcnt lgkmcnt(4)
	v_sub_u32_e32 v9, v37, v9
	v_lshl_add_u32 v45, v45, 13, v9
	v_add_lshl_u32 v45, v45, v16, 2
	s_waitcnt lgkmcnt(2)
	v_sub_u32_e32 v10, v38, v10
	v_lshl_add_u32 v46, v46, 13, v10
	v_add_lshl_u32 v46, v46, v17, 2
	s_waitcnt lgkmcnt(0)
	v_sub_u32_e32 v19, v39, v19

.Lw1b79:
	v_lshl_add_u32 v47, v47, 13, v19
	v_add_lshl_u32 v47, v47, v18, 2
	v_cmp_gt_i32_e64 s[36:37], s3, v32
	v_mov_b32_e32 v3, -1
	s_mov_b64 exec, s[36:37]
	global_load_dword v3, v40, s[28:29]
	s_mov_b64 exec, -1
	v_cmp_gt_i32_e64 s[38:39], s3, v33
	v_mov_b32_e32 v4, -1
	s_mov_b64 exec, s[38:39]

.Lw1b80:
	global_load_dword v4, v41, s[28:29]
	s_mov_b64 exec, -1
	v_cmp_gt_i32_e64 s[58:59], s3, v34
	v_mov_b32_e32 v6, -1
	s_mov_b64 exec, s[58:59]
	global_load_dword v6, v42, s[28:29]
	s_mov_b64 exec, -1
	v_cmp_gt_i32_e64 s[60:61], s3, v35
	v_mov_b32_e32 v7, -1
	s_mov_b64 exec, s[60:61]
	global_load_dword v7, v43, s[28:29]

.Lw1b81:
	s_mov_b64 exec, -1
	v_cmp_gt_i32_e64 s[36:37], s3, v36
	v_mov_b32_e32 v8, -1
	s_mov_b64 exec, s[36:37]
	global_load_dword v8, v44, s[28:29]
	s_mov_b64 exec, -1
	v_cmp_gt_i32_e64 s[38:39], s3, v37
	v_mov_b32_e32 v9, -1
	s_mov_b64 exec, s[38:39]
	global_load_dword v9, v45, s[28:29]

.Lw1b82:
	s_mov_b64 exec, -1
	v_cmp_gt_i32_e64 s[58:59], s3, v38
	v_mov_b32_e32 v10, -1
	s_mov_b64 exec, s[58:59]
	global_load_dword v10, v46, s[28:29]
	s_mov_b64 exec, -1
	v_cmp_gt_i32_e64 s[60:61], s3, v39
	v_mov_b32_e32 v13, -1
	s_mov_b64 exec, s[60:61]
	global_load_dword v13, v47, s[28:29]
	s_mov_b64 exec, -1

.Lw1b83:
	global_load_dwordx4 v[50:53], v58, s[68:69] nt
	global_load_dwordx4 v[54:57], v58, s[68:69] offset:1024 nt
	v_mov_b32_e32 v19, 1
	s_waitcnt vmcnt(9)
	v_cmp_ne_u32_e64 s[36:37], -1, v3
	v_lshrrev_b32_e32 v32, 15, v3
	v_and_b32_e32 v32, 0x1fffc, v32
	v_add_u32_e32 v32, 0x10000, v32
	v_mov_b32_e32 v15, 0
	s_mov_b64 exec, s[36:37]

.Lw1b84:
	ds_add_rtn_u32 v15, v32, v19
	s_mov_b64 exec, -1
	s_waitcnt vmcnt(8)
	v_cmp_ne_u32_e64 s[38:39], -1, v4
	v_lshrrev_b32_e32 v33, 15, v4
	v_and_b32_e32 v33, 0x1fffc, v33
	v_add_u32_e32 v33, 0x10000, v33
	v_mov_b32_e32 v5, 0
	s_mov_b64 exec, s[38:39]
	ds_add_rtn_u32 v5, v33, v19

.Lw1b85:
	s_mov_b64 exec, -1
	s_waitcnt vmcnt(7)
	v_cmp_ne_u32_e64 s[58:59], -1, v6
	v_lshrrev_b32_e32 v34, 15, v6
	v_and_b32_e32 v34, 0x1fffc, v34
	v_add_u32_e32 v34, 0x10000, v34
	v_mov_b32_e32 v16, 0
	s_mov_b64 exec, s[58:59]
	ds_add_rtn_u32 v16, v34, v19
	s_mov_b64 exec, -1
	s_waitcnt vmcnt(6)

.Lw1b86:
	v_cmp_ne_u32_e64 s[60:61], -1, v7
	v_lshrrev_b32_e32 v35, 15, v7
	v_and_b32_e32 v35, 0x1fffc, v35
	v_add_u32_e32 v35, 0x10000, v35
	v_mov_b32_e32 v11, 0
	s_mov_b64 exec, s[60:61]
	ds_add_rtn_u32 v11, v35, v19
	s_mov_b64 exec, -1
	s_waitcnt vmcnt(5)
	v_cmp_ne_u32_e64 s[36:37], -1, v8

.Lw1b87:
	v_lshrrev_b32_e32 v36, 15, v8
	v_and_b32_e32 v36, 0x1fffc, v36
	v_add_u32_e32 v36, 0x10000, v36
	v_mov_b32_e32 v17, 0
	s_mov_b64 exec, s[36:37]
	ds_add_rtn_u32 v17, v36, v19
	s_mov_b64 exec, -1
	s_waitcnt vmcnt(4)
	v_cmp_ne_u32_e64 s[38:39], -1, v9
	v_lshrrev_b32_e32 v37, 15, v9
	v_and_b32_e32 v37, 0x1fffc, v37

.Lw1b88:
	v_add_u32_e32 v37, 0x10000, v37
	v_mov_b32_e32 v12, 0
	s_mov_b64 exec, s[38:39]
	ds_add_rtn_u32 v12, v37, v19
	s_mov_b64 exec, -1
	s_waitcnt vmcnt(3)
	v_cmp_ne_u32_e64 s[58:59], -1, v10
	v_lshrrev_b32_e32 v38, 15, v10
	v_and_b32_e32 v38, 0x1fffc, v38
	v_add_u32_e32 v38, 0x10000, v38

.Lw1b89:
	v_mov_b32_e32 v18, 0
	s_mov_b64 exec, s[58:59]
	ds_add_rtn_u32 v18, v38, v19
	s_mov_b64 exec, -1
	s_waitcnt vmcnt(2)
	v_cmp_ne_u32_e64 s[60:61], -1, v13
	v_lshrrev_b32_e32 v39, 15, v13
	v_and_b32_e32 v39, 0x1fffc, v39
	v_add_u32_e32 v39, 0x10000, v39
	v_mov_b32_e32 v14, 0

.Lw1b90:
	s_mov_b64 exec, s[60:61]
	ds_add_rtn_u32 v14, v39, v19
	s_mov_b64 exec, -1
	s_waitcnt vmcnt(0)
	s_lshl_b32 s73, s72, 14
	s_add_u32 s70, s70, s73
	s_addc_u32 s71, s71, 0
	v_cmp_eq_u32_e64 s[36:37], 0, v59
	v_cvt_pk_f16_f32 v50, v50, v51
	v_cvt_pk_f16_f32 v51, v52, v53
	v_cvt_pk_f16_f32 v52, v54, v55

.Lw1b91:
	v_cvt_pk_f16_f32 v53, v56, v57
	v_cndmask_b32_e64 v54, v50, v52, s[36:37]
	v_cndmask_b32_e64 v55, v51, v53, s[36:37]
	s_nop 1
	v_mov_b32_dpp v54, v54 quad_perm:[1,0,3,2] row_mask:0xf bank_mask:0xf bound_ctrl:1
	v_mov_b32_dpp v55, v55 quad_perm:[1,0,3,2] row_mask:0xf bank_mask:0xf bound_ctrl:1
	v_cndmask_b32_e64 v50, v54, v50, s[36:37]
	v_cndmask_b32_e64 v51, v55, v51, s[36:37]

.Lw1b92:
	v_cndmask_b32_e64 v52, v52, v54, s[36:37]
	v_cndmask_b32_e64 v53, v53, v55, s[36:37]
	global_store_dwordx4 v49, v[50:53], s[70:71] sc1
	s_branch .LBB1_232

.Lmy_cvt1:
	s_waitcnt lgkmcnt(0)
	s_load_dwordx4 s[20:23], s[0:1], 0x28
	s_sub_i32 s3, s2, 392
	s_cmp_ge_u32 s3, 193
	s_cbranch_scc1 .Lmy_cvt1_end
	v_and_b32_e32 v1, 0x3c0, v0

.Lw1b157:
	v_and_b32_e32 v2, 63, v0
	v_lshlrev_b32_e32 v3, 5, v1
	v_lshl_or_b32 v3, v2, 4, v3
	v_and_b32_e32 v4, 1, v0
	v_lshrrev_b32_e32 v5, 1, v2
	v_lshl_or_b32 v5, v4, 5, v5
	v_add_u32_e32 v5, v5, v1
	v_lshlrev_b32_e32 v5, 4, v5
	v_cmp_eq_u32_e32 vcc, 0, v4
	s_waitcnt lgkmcnt(0)
	s_add_i32 s8, s3, 792
	s_lshl_b32 s9, s8, 10

.Lw1b158:
	s_sub_i32 s9, 0x1869c0, s9
	v_cmp_ge_i32_e64 s[24:25], s9, v1
	s_add_i32 s8, s3, 985
	s_lshl_b32 s9, s8, 10
	s_sub_i32 s9, 0x1869c0, s9
	v_cmp_ge_i32_e64 s[26:27], s9, v1
	s_add_i32 s8, s3, 1178
	s_lshl_b32 s9, s8, 10
	s_sub_i32 s9, 0x1869c0, s9

.Lw1b159:
	v_cmp_ge_i32_e64 s[28:29], s9, v1
	s_add_i32 s8, s3, 1371
	s_lshl_b32 s9, s8, 10
	s_sub_i32 s9, 0x1869c0, s9
	v_cmp_ge_i32_e64 s[30:31], s9, v1
	s_add_i32 s8, s3, 792
	s_lshl_b32 s9, s8, 15
	s_add_u32 s10, s20, s9
	s_addc_u32 s11, s21, 0

.Lw1b160:
	s_mov_b64 exec, s[24:25]
	global_load_dwordx4 v[8:11], v3, s[10:11] nt
	global_load_dwordx4 v[12:15], v3, s[10:11] offset:1024 nt
	s_add_i32 s8, s3, 985
	s_lshl_b32 s9, s8, 15
	s_add_u32 s10, s20, s9
	s_addc_u32 s11, s21, 0
	s_mov_b64 exec, s[26:27]
	global_load_dwordx4 v[16:19], v3, s[10:11] nt
	global_load_dwordx4 v[20:23], v3, s[10:11] offset:1024 nt

.Lw1b161:
	s_add_i32 s8, s3, 1178
	s_lshl_b32 s9, s8, 15
	s_add_u32 s10, s20, s9
	s_addc_u32 s11, s21, 0
	s_mov_b64 exec, s[28:29]
	global_load_dwordx4 v[24:27], v3, s[10:11] nt
	global_load_dwordx4 v[28:31], v3, s[10:11] offset:1024 nt
	s_add_i32 s8, s3, 1371
	s_lshl_b32 s9, s8, 15
	s_add_u32 s10, s20, s9
	s_addc_u32 s11, s21, 0

.Lw1b162:
	s_mov_b64 exec, s[30:31]
	global_load_dwordx4 v[32:35], v3, s[10:11] nt
	global_load_dwordx4 v[36:39], v3, s[10:11] offset:1024 nt
	s_waitcnt vmcnt(6)
	s_add_i32 s8, s3, 792
	s_lshl_b32 s9, s8, 14
	s_add_u32 s10, s22, s9
	s_addc_u32 s11, s23, 0
	s_mov_b64 exec, s[24:25]
	v_cvt_pk_f16_f32 v8, v8, v9
	v_cvt_pk_f16_f32 v9, v10, v11

.Lw1b164:
	v_cndmask_b32_e32 v11, v11, v13, vcc
	global_store_dwordx4 v5, v[8:11], s[10:11] sc1
	s_waitcnt vmcnt(5)
	s_add_i32 s8, s3, 985
	s_lshl_b32 s9, s8, 14
	s_add_u32 s10, s22, s9
	s_addc_u32 s11, s23, 0
	s_mov_b64 exec, s[26:27]
	v_cvt_pk_f16_f32 v16, v16, v17
	v_cvt_pk_f16_f32 v17, v18, v19
	v_cvt_pk_f16_f32 v18, v20, v21

.Lw1b166:
	s_waitcnt vmcnt(4)
	s_add_i32 s8, s3, 1178
	s_lshl_b32 s9, s8, 14
	s_add_u32 s10, s22, s9
	s_addc_u32 s11, s23, 0
	s_mov_b64 exec, s[28:29]
	v_cvt_pk_f16_f32 v24, v24, v25
	v_cvt_pk_f16_f32 v25, v26, v27
	v_cvt_pk_f16_f32 v26, v28, v29
	v_cvt_pk_f16_f32 v27, v30, v31

.Lw1b168:
	s_add_i32 s8, s3, 1371
	s_lshl_b32 s9, s8, 14
	s_add_u32 s10, s22, s9
	s_addc_u32 s11, s23, 0
	s_mov_b64 exec, s[30:31]
	v_cvt_pk_f16_f32 v32, v32, v33
	v_cvt_pk_f16_f32 v33, v34, v35
	v_cvt_pk_f16_f32 v34, v36, v37
	v_cvt_pk_f16_f32 v35, v38, v39
	v_cndmask_b32_e32 v36, v32, v34, vcc

	.amdhsa_kernel _Z8k_bucketPKiS0_PKjPiS3_PK15HIP_vector_typeIfLj4EEPS4_IjLj4EE
		.amdhsa_group_segment_fixed_size 72624
		.amdhsa_private_segment_fixed_size 0
		.amdhsa_kernarg_size 56
		.amdhsa_user_sgpr_count 2
		.amdhsa_user_sgpr_dispatch_ptr 0
		.amdhsa_user_sgpr_queue_ptr 0
		.amdhsa_user_sgpr_kernarg_segment_ptr 1
		.amdhsa_user_sgpr_dispatch_id 0
		.amdhsa_user_sgpr_kernarg_preload_length 0
		.amdhsa_user_sgpr_kernarg_preload_offset 0
		.amdhsa_user_sgpr_private_segment_size 0
		.amdhsa_uses_dynamic_stack 0
		.amdhsa_enable_private_segment 0
		.amdhsa_system_sgpr_workgroup_id_x 1
		.amdhsa_system_sgpr_workgroup_id_y 0
		.amdhsa_system_sgpr_workgroup_id_z 0
		.amdhsa_system_sgpr_workgroup_info 0
		.amdhsa_system_vgpr_workitem_id 0
		.amdhsa_next_free_vgpr 60
		.amdhsa_next_free_sgpr 74
		.amdhsa_accum_offset 60
		.amdhsa_reserve_vcc 1
		.amdhsa_float_round_mode_32 0
		.amdhsa_float_round_mode_16_64 0
		.amdhsa_float_denorm_mode_32 3
		.amdhsa_float_denorm_mode_16_64 3
		.amdhsa_dx10_clamp 1
		.amdhsa_ieee_mode 1
		.amdhsa_fp16_overflow 0
		.amdhsa_tg_split 0
		.amdhsa_exception_fp_ieee_invalid_op 0
		.amdhsa_exception_fp_denorm_src 0
		.amdhsa_exception_fp_ieee_div_zero 0
		.amdhsa_exception_fp_ieee_overflow 0
		.amdhsa_exception_fp_ieee_underflow 0
		.amdhsa_exception_fp_ieee_inexact 0
		.amdhsa_exception_int_div_zero 0
	.end_amdhsa_kernel

amdhsa.kernels:
  - .agpr_count:     0
    .args:
      - .actual_access:  read_only
        .address_space:  global
        .offset:         0
        .size:           8
        .value_kind:     global_buffer
      - .actual_access:  read_only
        .address_space:  global
        .offset:         8
        .size:           8
        .value_kind:     global_buffer
      - .actual_access:  write_only
        .address_space:  global
        .offset:         16
        .size:           8
        .value_kind:     global_buffer
      - .actual_access:  write_only
        .address_space:  global
        .offset:         24
        .size:           8
        .value_kind:     global_buffer
      - .actual_access:  write_only
        .address_space:  global
        .offset:         32
        .size:           8
        .value_kind:     global_buffer
      - .actual_access:  read_only
        .address_space:  global
        .offset:         40
        .size:           8
        .value_kind:     global_buffer
      - .actual_access:  read_only
        .address_space:  global
        .offset:         48
        .size:           8
        .value_kind:     global_buffer
      - .actual_access:  read_only
        .address_space:  global
        .offset:         56
        .size:           8
        .value_kind:     global_buffer
      - .actual_access:  write_only
        .address_space:  global
        .offset:         64
        .size:           8
        .value_kind:     global_buffer
      - .actual_access:  write_only
        .address_space:  global
        .offset:         72
        .size:           8
        .value_kind:     global_buffer
      - .actual_access:  read_only
        .address_space:  global
        .offset:         80
        .size:           8
        .value_kind:     global_buffer
      - .address_space:  global
        .offset:         88
        .size:           8
        .value_kind:     global_buffer
      - .actual_access:  write_only
        .address_space:  global
        .offset:         96
        .size:           8
        .value_kind:     global_buffer
    .group_segment_fixed_size: 34400
    .kernarg_segment_align: 8
    .kernarg_segment_size: 104
    .language:       OpenCL C
    .language_version:
      - 2
      - 0
    .max_flat_workgroup_size: 1024
    .name:           _Z7k_frontPKiS0_PiS1_PjPKfS4_S4_P15HIP_vector_typeIjLj4EES7_PKS5_IfLj4EES7_S7_
    .private_segment_fixed_size: 0
    .sgpr_count:     44
    .sgpr_spill_count: 0
    .symbol:         _Z7k_frontPKiS0_PiS1_PjPKfS4_S4_P15HIP_vector_typeIjLj4EES7_PKS5_IfLj4EES7_S7_.kd
    .uniform_work_group_size: 1
    .uses_dynamic_stack: false
    .vgpr_count:     41
    .vgpr_spill_count: 0
    .wavefront_size: 64
  - .agpr_count:     0
    .args:
      - .actual_access:  read_only
        .address_space:  global
        .offset:         0
        .size:           8
        .value_kind:     global_buffer
      - .actual_access:  read_only
        .address_space:  global
        .offset:         8
        .size:           8
        .value_kind:     global_buffer
      - .actual_access:  read_only
        .address_space:  global
        .offset:         16
        .size:           8
        .value_kind:     global_buffer
      - .actual_access:  write_only
        .address_space:  global
        .offset:         24
        .size:           8
        .value_kind:     global_buffer
      - .address_space:  global
        .offset:         32
        .size:           8
        .value_kind:     global_buffer
      - .actual_access:  read_only
        .address_space:  global
        .offset:         40
        .size:           8
        .value_kind:     global_buffer
      - .address_space:  global
        .offset:         48
        .size:           8
        .value_kind:     global_buffer
    .group_segment_fixed_size: 72624
    .kernarg_segment_align: 8
    .kernarg_segment_size: 56
    .language:       OpenCL C
    .language_version:
      - 2
      - 0
    .max_flat_workgroup_size: 1024
    .name:           _Z8k_bucketPKiS0_PKjPiS3_PK15HIP_vector_typeIfLj4EEPS4_IjLj4EE
    .private_segment_fixed_size: 0
    .sgpr_count:     80
    .sgpr_spill_count: 0
    .symbol:         _Z8k_bucketPKiS0_PKjPiS3_PK15HIP_vector_typeIfLj4EEPS4_IjLj4EE.kd
    .uniform_work_group_size: 1
    .uses_dynamic_stack: false
    .vgpr_count:     60
    .vgpr_spill_count: 0
    .wavefront_size: 64
  - .agpr_count:     0
    .args:
      - .actual_access:  read_only
        .address_space:  global
        .offset:         0
        .size:           8
        .value_kind:     global_buffer
      - .actual_access:  read_only
        .address_space:  global
        .offset:         8
        .size:           8
        .value_kind:     global_buffer
      - .actual_access:  read_only
        .address_space:  global
        .offset:         16
        .size:           8
        .value_kind:     global_buffer
      - .actual_access:  read_only
        .address_space:  global
        .offset:         24
        .size:           8
        .value_kind:     global_buffer
      - .actual_access:  read_only
        .address_space:  global
        .offset:         32
        .size:           8
        .value_kind:     global_buffer
      - .actual_access:  read_only
        .address_space:  global
        .offset:         40
        .size:           8
        .value_kind:     global_buffer
      - .actual_access:  read_only
        .address_space:  global
        .offset:         48
        .size:           8
        .value_kind:     global_buffer
      - .actual_access:  read_only
        .address_space:  global
        .offset:         56
        .size:           8
        .value_kind:     global_buffer
      - .actual_access:  read_only
        .address_space:  global
        .offset:         64
        .size:           8
        .value_kind:     global_buffer
      - .actual_access:  read_only
        .address_space:  global
        .offset:         72
        .size:           8
        .value_kind:     global_buffer
      - .actual_access:  read_only
        .address_space:  global
        .offset:         80
        .size:           8
        .value_kind:     global_buffer
      - .actual_access:  write_only
        .address_space:  global
        .offset:         88
        .size:           8
        .value_kind:     global_buffer
      - .actual_access:  read_only
        .address_space:  global
        .offset:         96
        .size:           8
        .value_kind:     global_buffer
      - .offset:         104
        .size:           4
        .value_kind:     hidden_block_count_x
      - .offset:         108
        .size:           4
        .value_kind:     hidden_block_count_y
      - .offset:         112
        .size:           4
        .value_kind:     hidden_block_count_z
      - .offset:         116
        .size:           2
        .value_kind:     hidden_group_size_x
      - .offset:         118
        .size:           2
        .value_kind:     hidden_group_size_y
      - .offset:         120
        .size:           2
        .value_kind:     hidden_group_size_z
      - .offset:         122
        .size:           2
        .value_kind:     hidden_remainder_x
      - .offset:         124
        .size:           2
        .value_kind:     hidden_remainder_y
      - .offset:         126
        .size:           2
        .value_kind:     hidden_remainder_z
      - .offset:         144
        .size:           8
        .value_kind:     hidden_global_offset_x
      - .offset:         152
        .size:           8
        .value_kind:     hidden_global_offset_y
      - .offset:         160
        .size:           8
        .value_kind:     hidden_global_offset_z
      - .offset:         168
        .size:           2
        .value_kind:     hidden_grid_dims
    .group_segment_fixed_size: 125188
    .kernarg_segment_align: 8
    .kernarg_segment_size: 360
    .language:       OpenCL C
    .language_version:
      - 2
      - 0
    .max_flat_workgroup_size: 832
    .name:           _Z10k_layer_a2ILi0ELi13EEvPKDF16_PKiS3_PK15HIP_vector_typeIjLj4EES7_PKfS9_S9_S9_S9_S9_PDF16_Pf
    .private_segment_fixed_size: 0
    .sgpr_count:     58
    .sgpr_spill_count: 0
    .symbol:         _Z10k_layer_a2ILi0ELi13EEvPKDF16_PKiS3_PK15HIP_vector_typeIjLj4EES7_PKfS9_S9_S9_S9_S9_PDF16_Pf.kd
    .uniform_work_group_size: 1
    .uses_dynamic_stack: false
    .vgpr_count:     128
    .vgpr_spill_count: 0
    .wavefront_size: 64
  - .agpr_count:     0
    .args:
      - .actual_access:  read_only
        .address_space:  global
        .offset:         0
        .size:           8
        .value_kind:     global_buffer
      - .actual_access:  read_only
        .address_space:  global
        .offset:         8
        .size:           8
        .value_kind:     global_buffer
      - .actual_access:  read_only
        .address_space:  global
        .offset:         16
        .size:           8
        .value_kind:     global_buffer
      - .actual_access:  read_only
        .address_space:  global
        .offset:         24
        .size:           8
        .value_kind:     global_buffer
      - .actual_access:  read_only
        .address_space:  global
        .offset:         32
        .size:           8
        .value_kind:     global_buffer
      - .actual_access:  read_only
        .address_space:  global
        .offset:         40
        .size:           8
        .value_kind:     global_buffer
      - .actual_access:  read_only
        .address_space:  global
        .offset:         48
        .size:           8
        .value_kind:     global_buffer
      - .actual_access:  read_only
        .address_space:  global
        .offset:         56
        .size:           8
        .value_kind:     global_buffer
      - .actual_access:  read_only
        .address_space:  global
        .offset:         64
        .size:           8
        .value_kind:     global_buffer
      - .actual_access:  read_only
        .address_space:  global
        .offset:         72
        .size:           8
        .value_kind:     global_buffer
      - .actual_access:  read_only
        .address_space:  global
        .offset:         80
        .size:           8
        .value_kind:     global_buffer
      - .actual_access:  read_only
        .address_space:  global
        .offset:         88
        .size:           8
        .value_kind:     global_buffer
      - .actual_access:  write_only
        .address_space:  global
        .offset:         96
        .size:           8
        .value_kind:     global_buffer
      - .offset:         104
        .size:           4
        .value_kind:     hidden_block_count_x
      - .offset:         108
        .size:           4
        .value_kind:     hidden_block_count_y
      - .offset:         112
        .size:           4
        .value_kind:     hidden_block_count_z
      - .offset:         116
        .size:           2
        .value_kind:     hidden_group_size_x
      - .offset:         118
        .size:           2
        .value_kind:     hidden_group_size_y
      - .offset:         120
        .size:           2
        .value_kind:     hidden_group_size_z
      - .offset:         122
        .size:           2
        .value_kind:     hidden_remainder_x
      - .offset:         124
        .size:           2
        .value_kind:     hidden_remainder_y
      - .offset:         126
        .size:           2
        .value_kind:     hidden_remainder_z
      - .offset:         144
        .size:           8
        .value_kind:     hidden_global_offset_x
      - .offset:         152
        .size:           8
        .value_kind:     hidden_global_offset_y
      - .offset:         160
        .size:           8
        .value_kind:     hidden_global_offset_z
      - .offset:         168
        .size:           2
        .value_kind:     hidden_grid_dims
    .group_segment_fixed_size: 162052
    .kernarg_segment_align: 8
    .kernarg_segment_size: 360
    .language:       OpenCL C
    .language_version:
      - 2
      - 0
    .max_flat_workgroup_size: 832
    .name:           _Z10k_layer_a2ILi1ELi13EEvPKDF16_PKiS3_PK15HIP_vector_typeIjLj4EES7_PKfS9_S9_S9_S9_S9_PDF16_Pf
    .private_segment_fixed_size: 0
    .sgpr_count:     58
    .sgpr_spill_count: 0
    .symbol:         _Z10k_layer_a2ILi1ELi13EEvPKDF16_PKiS3_PK15HIP_vector_typeIjLj4EES7_PKfS9_S9_S9_S9_S9_PDF16_Pf.kd
    .uniform_work_group_size: 1
    .uses_dynamic_stack: false
    .vgpr_count:     125
    .vgpr_spill_count: 0
    .wavefront_size: 64
